# mixer pooling matmul k-loop unrolled with prefetched weight fragments + double-buffered LDS reads; GEMM2 epilogue LDS table reads hoisted (one wait per unit)
# speedup vs baseline: 1.0421x; 1.0002x over previous
.LBB0_539:
	v_add_co_u32_e32 v148, vcc, s20, v74
	s_nop 1
	v_addc_co_u32_e32 v149, vcc, 0, v75, vcc
	v_add_co_u32_e32 v150, vcc, s20, v72
	s_nop 1
	v_addc_co_u32_e32 v151, vcc, 0, v73, vcc
	global_load_dwordx4 v[210:213], v[148:149], off
	global_load_dwordx4 v[214:217], v[150:151], off
	global_load_dwordx4 v[218:221], v[148:149], off offset:64
	global_load_dwordx4 v[222:225], v[150:151], off offset:64
	global_load_dwordx4 v[226:229], v[148:149], off offset:128
	global_load_dwordx4 v[230:233], v[150:151], off offset:128
	global_load_dwordx4 v[234:237], v[148:149], off offset:192
	global_load_dwordx4 v[238:241], v[150:151], off offset:192
	v_xor_b32_e32 v78, v203, v159
	v_lshl_add_u32 v133, v78, 4, v76
	ds_read_b128 v[144:147], v133
	ds_read_b128 v[244:247], v133 offset:8192
	v_add_u32_e32 v78, 4, v203
	v_xor_b32_e32 v78, v78, v159
	v_lshl_add_u32 v79, v78, 4, v76
	s_waitcnt vmcnt(6) lgkmcnt(1)
	v_mfma_f32_16x16x32_bf16 v[100:103], v[210:213], v[144:147], v[100:103]
	v_mfma_f32_16x16x32_bf16 v[96:99], v[214:217], v[144:147], v[96:99]
	ds_read_b128 v[144:147], v133 offset:16384
	s_waitcnt lgkmcnt(1)
	v_mfma_f32_16x16x32_bf16 v[92:95], v[210:213], v[244:247], v[92:95]
	v_mfma_f32_16x16x32_bf16 v[88:91], v[214:217], v[244:247], v[88:91]
	ds_read_b128 v[244:247], v133 offset:24576
	s_waitcnt lgkmcnt(1)
	v_mfma_f32_16x16x32_bf16 v[84:87], v[210:213], v[144:147], v[84:87]
	v_mfma_f32_16x16x32_bf16 v[80:83], v[214:217], v[144:147], v[80:83]
	ds_read_b128 v[144:147], v133 offset:32768
	s_waitcnt lgkmcnt(1)
	v_mfma_f32_16x16x32_bf16 v[68:71], v[210:213], v[244:247], v[68:71]
	v_mfma_f32_16x16x32_bf16 v[64:67], v[214:217], v[244:247], v[64:67]
	ds_read_b128 v[244:247], v133 offset:40960
	s_waitcnt lgkmcnt(1)
	v_mfma_f32_16x16x32_bf16 v[60:63], v[210:213], v[144:147], v[60:63]
	v_mfma_f32_16x16x32_bf16 v[56:59], v[214:217], v[144:147], v[56:59]
	ds_read_b128 v[144:147], v133 offset:49152
	s_waitcnt lgkmcnt(1)
	v_mfma_f32_16x16x32_bf16 v[52:55], v[210:213], v[244:247], v[52:55]
	v_mfma_f32_16x16x32_bf16 v[48:51], v[214:217], v[244:247], v[48:51]
	ds_read_b128 v[244:247], v133 offset:57344
	s_waitcnt lgkmcnt(1)
	v_mfma_f32_16x16x32_bf16 v[44:47], v[210:213], v[144:147], v[44:47]
	v_mfma_f32_16x16x32_bf16 v[40:43], v[214:217], v[144:147], v[40:43]
	ds_read_b128 v[144:147], v79
	s_waitcnt lgkmcnt(1)
	v_mfma_f32_16x16x32_bf16 v[36:39], v[210:213], v[244:247], v[36:39]
	v_mfma_f32_16x16x32_bf16 v[32:35], v[214:217], v[244:247], v[32:35]
	ds_read_b128 v[244:247], v79 offset:8192
	global_load_dwordx4 v[210:213], v[148:149], off offset:256
	global_load_dwordx4 v[214:217], v[150:151], off offset:256
	v_add_u32_e32 v78, 8, v203
	v_xor_b32_e32 v78, v78, v159
	v_lshl_add_u32 v133, v78, 4, v76
	s_waitcnt vmcnt(6) lgkmcnt(1)
	v_mfma_f32_16x16x32_bf16 v[100:103], v[218:221], v[144:147], v[100:103]
	v_mfma_f32_16x16x32_bf16 v[96:99], v[222:225], v[144:147], v[96:99]
	ds_read_b128 v[144:147], v79 offset:16384
	s_waitcnt lgkmcnt(1)
	v_mfma_f32_16x16x32_bf16 v[92:95], v[218:221], v[244:247], v[92:95]
	v_mfma_f32_16x16x32_bf16 v[88:91], v[222:225], v[244:247], v[88:91]
	ds_read_b128 v[244:247], v79 offset:24576
	s_waitcnt lgkmcnt(1)
	v_mfma_f32_16x16x32_bf16 v[84:87], v[218:221], v[144:147], v[84:87]
	v_mfma_f32_16x16x32_bf16 v[80:83], v[222:225], v[144:147], v[80:83]
	ds_read_b128 v[144:147], v79 offset:32768
	s_waitcnt lgkmcnt(1)
	v_mfma_f32_16x16x32_bf16 v[68:71], v[218:221], v[244:247], v[68:71]
	v_mfma_f32_16x16x32_bf16 v[64:67], v[222:225], v[244:247], v[64:67]
	ds_read_b128 v[244:247], v79 offset:40960
	s_waitcnt lgkmcnt(1)
	v_mfma_f32_16x16x32_bf16 v[60:63], v[218:221], v[144:147], v[60:63]
	v_mfma_f32_16x16x32_bf16 v[56:59], v[222:225], v[144:147], v[56:59]
	ds_read_b128 v[144:147], v79 offset:49152
	s_waitcnt lgkmcnt(1)
	v_mfma_f32_16x16x32_bf16 v[52:55], v[218:221], v[244:247], v[52:55]
	v_mfma_f32_16x16x32_bf16 v[48:51], v[222:225], v[244:247], v[48:51]
	ds_read_b128 v[244:247], v79 offset:57344
	s_waitcnt lgkmcnt(1)
	v_mfma_f32_16x16x32_bf16 v[44:47], v[218:221], v[144:147], v[44:47]
	v_mfma_f32_16x16x32_bf16 v[40:43], v[222:225], v[144:147], v[40:43]
	ds_read_b128 v[144:147], v133
	s_waitcnt lgkmcnt(1)
	v_mfma_f32_16x16x32_bf16 v[36:39], v[218:221], v[244:247], v[36:39]
	v_mfma_f32_16x16x32_bf16 v[32:35], v[222:225], v[244:247], v[32:35]
	ds_read_b128 v[244:247], v133 offset:8192
	global_load_dwordx4 v[218:221], v[148:149], off offset:320
	global_load_dwordx4 v[222:225], v[150:151], off offset:320
	v_add_u32_e32 v78, 12, v203
	v_xor_b32_e32 v78, v78, v159
	v_lshl_add_u32 v79, v78, 4, v76
	s_waitcnt vmcnt(6) lgkmcnt(1)
	v_mfma_f32_16x16x32_bf16 v[100:103], v[226:229], v[144:147], v[100:103]
	v_mfma_f32_16x16x32_bf16 v[96:99], v[230:233], v[144:147], v[96:99]
	ds_read_b128 v[144:147], v133 offset:16384
	s_waitcnt lgkmcnt(1)
	v_mfma_f32_16x16x32_bf16 v[92:95], v[226:229], v[244:247], v[92:95]
	v_mfma_f32_16x16x32_bf16 v[88:91], v[230:233], v[244:247], v[88:91]
	ds_read_b128 v[244:247], v133 offset:24576
	s_waitcnt lgkmcnt(1)
	v_mfma_f32_16x16x32_bf16 v[84:87], v[226:229], v[144:147], v[84:87]
	v_mfma_f32_16x16x32_bf16 v[80:83], v[230:233], v[144:147], v[80:83]
	ds_read_b128 v[144:147], v133 offset:32768
	s_waitcnt lgkmcnt(1)
	v_mfma_f32_16x16x32_bf16 v[68:71], v[226:229], v[244:247], v[68:71]
	v_mfma_f32_16x16x32_bf16 v[64:67], v[230:233], v[244:247], v[64:67]
	ds_read_b128 v[244:247], v133 offset:40960
	s_waitcnt lgkmcnt(1)
	v_mfma_f32_16x16x32_bf16 v[60:63], v[226:229], v[144:147], v[60:63]
	v_mfma_f32_16x16x32_bf16 v[56:59], v[230:233], v[144:147], v[56:59]
	ds_read_b128 v[144:147], v133 offset:49152
	s_waitcnt lgkmcnt(1)
	v_mfma_f32_16x16x32_bf16 v[52:55], v[226:229], v[244:247], v[52:55]
	v_mfma_f32_16x16x32_bf16 v[48:51], v[230:233], v[244:247], v[48:51]
	ds_read_b128 v[244:247], v133 offset:57344
	s_waitcnt lgkmcnt(1)
	v_mfma_f32_16x16x32_bf16 v[44:47], v[226:229], v[144:147], v[44:47]
	v_mfma_f32_16x16x32_bf16 v[40:43], v[230:233], v[144:147], v[40:43]
	ds_read_b128 v[144:147], v79
	s_waitcnt lgkmcnt(1)
	v_mfma_f32_16x16x32_bf16 v[36:39], v[226:229], v[244:247], v[36:39]
	v_mfma_f32_16x16x32_bf16 v[32:35], v[230:233], v[244:247], v[32:35]
	ds_read_b128 v[244:247], v79 offset:8192
	global_load_dwordx4 v[226:229], v[148:149], off offset:384
	global_load_dwordx4 v[230:233], v[150:151], off offset:384
	v_add_u32_e32 v78, 16, v203
	v_xor_b32_e32 v78, v78, v159
	v_lshl_add_u32 v133, v78, 4, v76
	s_waitcnt vmcnt(6) lgkmcnt(1)
	v_mfma_f32_16x16x32_bf16 v[100:103], v[234:237], v[144:147], v[100:103]
	v_mfma_f32_16x16x32_bf16 v[96:99], v[238:241], v[144:147], v[96:99]
	ds_read_b128 v[144:147], v79 offset:16384
	s_waitcnt lgkmcnt(1)
	v_mfma_f32_16x16x32_bf16 v[92:95], v[234:237], v[244:247], v[92:95]
	v_mfma_f32_16x16x32_bf16 v[88:91], v[238:241], v[244:247], v[88:91]
	ds_read_b128 v[244:247], v79 offset:24576
	s_waitcnt lgkmcnt(1)
	v_mfma_f32_16x16x32_bf16 v[84:87], v[234:237], v[144:147], v[84:87]
	v_mfma_f32_16x16x32_bf16 v[80:83], v[238:241], v[144:147], v[80:83]
	ds_read_b128 v[144:147], v79 offset:32768
	s_waitcnt lgkmcnt(1)
	v_mfma_f32_16x16x32_bf16 v[68:71], v[234:237], v[244:247], v[68:71]
	v_mfma_f32_16x16x32_bf16 v[64:67], v[238:241], v[244:247], v[64:67]
	ds_read_b128 v[244:247], v79 offset:40960
	s_waitcnt lgkmcnt(1)
	v_mfma_f32_16x16x32_bf16 v[60:63], v[234:237], v[144:147], v[60:63]
	v_mfma_f32_16x16x32_bf16 v[56:59], v[238:241], v[144:147], v[56:59]
	ds_read_b128 v[144:147], v79 offset:49152
	s_waitcnt lgkmcnt(1)
	v_mfma_f32_16x16x32_bf16 v[52:55], v[234:237], v[244:247], v[52:55]
	v_mfma_f32_16x16x32_bf16 v[48:51], v[238:241], v[244:247], v[48:51]
	ds_read_b128 v[244:247], v79 offset:57344
	s_waitcnt lgkmcnt(1)
	v_mfma_f32_16x16x32_bf16 v[44:47], v[234:237], v[144:147], v[44:47]
	v_mfma_f32_16x16x32_bf16 v[40:43], v[238:241], v[144:147], v[40:43]
	ds_read_b128 v[144:147], v133
	s_waitcnt lgkmcnt(1)
	v_mfma_f32_16x16x32_bf16 v[36:39], v[234:237], v[244:247], v[36:39]
	v_mfma_f32_16x16x32_bf16 v[32:35], v[238:241], v[244:247], v[32:35]
	ds_read_b128 v[244:247], v133 offset:8192
	global_load_dwordx4 v[234:237], v[148:149], off offset:448
	global_load_dwordx4 v[238:241], v[150:151], off offset:448
	v_add_u32_e32 v78, 20, v203
	v_xor_b32_e32 v78, v78, v159
	v_lshl_add_u32 v79, v78, 4, v76
	s_waitcnt vmcnt(6) lgkmcnt(1)
	v_mfma_f32_16x16x32_bf16 v[100:103], v[210:213], v[144:147], v[100:103]
	v_mfma_f32_16x16x32_bf16 v[96:99], v[214:217], v[144:147], v[96:99]
	ds_read_b128 v[144:147], v133 offset:16384
	s_waitcnt lgkmcnt(1)
	v_mfma_f32_16x16x32_bf16 v[92:95], v[210:213], v[244:247], v[92:95]
	v_mfma_f32_16x16x32_bf16 v[88:91], v[214:217], v[244:247], v[88:91]
	ds_read_b128 v[244:247], v133 offset:24576
	s_waitcnt lgkmcnt(1)
	v_mfma_f32_16x16x32_bf16 v[84:87], v[210:213], v[144:147], v[84:87]
	v_mfma_f32_16x16x32_bf16 v[80:83], v[214:217], v[144:147], v[80:83]
	ds_read_b128 v[144:147], v133 offset:32768
	s_waitcnt lgkmcnt(1)
	v_mfma_f32_16x16x32_bf16 v[68:71], v[210:213], v[244:247], v[68:71]
	v_mfma_f32_16x16x32_bf16 v[64:67], v[214:217], v[244:247], v[64:67]
	ds_read_b128 v[244:247], v133 offset:40960
	s_waitcnt lgkmcnt(1)
	v_mfma_f32_16x16x32_bf16 v[60:63], v[210:213], v[144:147], v[60:63]
	v_mfma_f32_16x16x32_bf16 v[56:59], v[214:217], v[144:147], v[56:59]
	ds_read_b128 v[144:147], v133 offset:49152
	s_waitcnt lgkmcnt(1)
	v_mfma_f32_16x16x32_bf16 v[52:55], v[210:213], v[244:247], v[52:55]
	v_mfma_f32_16x16x32_bf16 v[48:51], v[214:217], v[244:247], v[48:51]
	ds_read_b128 v[244:247], v133 offset:57344
	s_waitcnt lgkmcnt(1)
	v_mfma_f32_16x16x32_bf16 v[44:47], v[210:213], v[144:147], v[44:47]
	v_mfma_f32_16x16x32_bf16 v[40:43], v[214:217], v[144:147], v[40:43]
	ds_read_b128 v[144:147], v79
	s_waitcnt lgkmcnt(1)
	v_mfma_f32_16x16x32_bf16 v[36:39], v[210:213], v[244:247], v[36:39]
	v_mfma_f32_16x16x32_bf16 v[32:35], v[214:217], v[244:247], v[32:35]
	ds_read_b128 v[244:247], v79 offset:8192
	v_add_u32_e32 v78, 24, v203
	v_xor_b32_e32 v78, v78, v159
	v_lshl_add_u32 v133, v78, 4, v76
	s_waitcnt vmcnt(4) lgkmcnt(1)
	v_mfma_f32_16x16x32_bf16 v[100:103], v[218:221], v[144:147], v[100:103]
	v_mfma_f32_16x16x32_bf16 v[96:99], v[222:225], v[144:147], v[96:99]
	ds_read_b128 v[144:147], v79 offset:16384
	s_waitcnt lgkmcnt(1)
	v_mfma_f32_16x16x32_bf16 v[92:95], v[218:221], v[244:247], v[92:95]
	v_mfma_f32_16x16x32_bf16 v[88:91], v[222:225], v[244:247], v[88:91]
	ds_read_b128 v[244:247], v79 offset:24576
	s_waitcnt lgkmcnt(1)
	v_mfma_f32_16x16x32_bf16 v[84:87], v[218:221], v[144:147], v[84:87]
	v_mfma_f32_16x16x32_bf16 v[80:83], v[222:225], v[144:147], v[80:83]
	ds_read_b128 v[144:147], v79 offset:32768
	s_waitcnt lgkmcnt(1)
	v_mfma_f32_16x16x32_bf16 v[68:71], v[218:221], v[244:247], v[68:71]
	v_mfma_f32_16x16x32_bf16 v[64:67], v[222:225], v[244:247], v[64:67]
	ds_read_b128 v[244:247], v79 offset:40960
	s_waitcnt lgkmcnt(1)
	v_mfma_f32_16x16x32_bf16 v[60:63], v[218:221], v[144:147], v[60:63]
	v_mfma_f32_16x16x32_bf16 v[56:59], v[222:225], v[144:147], v[56:59]
	ds_read_b128 v[144:147], v79 offset:49152
	s_waitcnt lgkmcnt(1)
	v_mfma_f32_16x16x32_bf16 v[52:55], v[218:221], v[244:247], v[52:55]
	v_mfma_f32_16x16x32_bf16 v[48:51], v[222:225], v[244:247], v[48:51]
	ds_read_b128 v[244:247], v79 offset:57344
	s_waitcnt lgkmcnt(1)
	v_mfma_f32_16x16x32_bf16 v[44:47], v[218:221], v[144:147], v[44:47]
	v_mfma_f32_16x16x32_bf16 v[40:43], v[222:225], v[144:147], v[40:43]
	ds_read_b128 v[144:147], v133
	s_waitcnt lgkmcnt(1)
	v_mfma_f32_16x16x32_bf16 v[36:39], v[218:221], v[244:247], v[36:39]
	v_mfma_f32_16x16x32_bf16 v[32:35], v[222:225], v[244:247], v[32:35]
	ds_read_b128 v[244:247], v133 offset:8192
	v_add_u32_e32 v78, 28, v203
	v_xor_b32_e32 v78, v78, v159
	v_lshl_add_u32 v79, v78, 4, v76
	s_waitcnt vmcnt(2) lgkmcnt(1)
	v_mfma_f32_16x16x32_bf16 v[100:103], v[226:229], v[144:147], v[100:103]
	v_mfma_f32_16x16x32_bf16 v[96:99], v[230:233], v[144:147], v[96:99]
	ds_read_b128 v[144:147], v133 offset:16384
	s_waitcnt lgkmcnt(1)
	v_mfma_f32_16x16x32_bf16 v[92:95], v[226:229], v[244:247], v[92:95]
	v_mfma_f32_16x16x32_bf16 v[88:91], v[230:233], v[244:247], v[88:91]
	ds_read_b128 v[244:247], v133 offset:24576
	s_waitcnt lgkmcnt(1)
	v_mfma_f32_16x16x32_bf16 v[84:87], v[226:229], v[144:147], v[84:87]
	v_mfma_f32_16x16x32_bf16 v[80:83], v[230:233], v[144:147], v[80:83]
	ds_read_b128 v[144:147], v133 offset:32768
	s_waitcnt lgkmcnt(1)
	v_mfma_f32_16x16x32_bf16 v[68:71], v[226:229], v[244:247], v[68:71]
	v_mfma_f32_16x16x32_bf16 v[64:67], v[230:233], v[244:247], v[64:67]
	ds_read_b128 v[244:247], v133 offset:40960
	s_waitcnt lgkmcnt(1)
	v_mfma_f32_16x16x32_bf16 v[60:63], v[226:229], v[144:147], v[60:63]
	v_mfma_f32_16x16x32_bf16 v[56:59], v[230:233], v[144:147], v[56:59]
	ds_read_b128 v[144:147], v133 offset:49152
	s_waitcnt lgkmcnt(1)
	v_mfma_f32_16x16x32_bf16 v[52:55], v[226:229], v[244:247], v[52:55]
	v_mfma_f32_16x16x32_bf16 v[48:51], v[230:233], v[244:247], v[48:51]
	ds_read_b128 v[244:247], v133 offset:57344
	s_waitcnt lgkmcnt(1)
	v_mfma_f32_16x16x32_bf16 v[44:47], v[226:229], v[144:147], v[44:47]
	v_mfma_f32_16x16x32_bf16 v[40:43], v[230:233], v[144:147], v[40:43]
	ds_read_b128 v[144:147], v79
	s_waitcnt lgkmcnt(1)
	v_mfma_f32_16x16x32_bf16 v[36:39], v[226:229], v[244:247], v[36:39]
	v_mfma_f32_16x16x32_bf16 v[32:35], v[230:233], v[244:247], v[32:35]
	ds_read_b128 v[244:247], v79 offset:8192
	s_waitcnt vmcnt(0) lgkmcnt(1)
	v_mfma_f32_16x16x32_bf16 v[100:103], v[234:237], v[144:147], v[100:103]
	v_mfma_f32_16x16x32_bf16 v[96:99], v[238:241], v[144:147], v[96:99]
	ds_read_b128 v[144:147], v79 offset:16384
	s_waitcnt lgkmcnt(1)
	v_mfma_f32_16x16x32_bf16 v[92:95], v[234:237], v[244:247], v[92:95]
	v_mfma_f32_16x16x32_bf16 v[88:91], v[238:241], v[244:247], v[88:91]
	ds_read_b128 v[244:247], v79 offset:24576
	s_waitcnt lgkmcnt(1)
	v_mfma_f32_16x16x32_bf16 v[84:87], v[234:237], v[144:147], v[84:87]
	v_mfma_f32_16x16x32_bf16 v[80:83], v[238:241], v[144:147], v[80:83]
	ds_read_b128 v[144:147], v79 offset:32768
	s_waitcnt lgkmcnt(1)
	v_mfma_f32_16x16x32_bf16 v[68:71], v[234:237], v[244:247], v[68:71]
	v_mfma_f32_16x16x32_bf16 v[64:67], v[238:241], v[244:247], v[64:67]
	ds_read_b128 v[244:247], v79 offset:40960
	s_waitcnt lgkmcnt(1)
	v_mfma_f32_16x16x32_bf16 v[60:63], v[234:237], v[144:147], v[60:63]
	v_mfma_f32_16x16x32_bf16 v[56:59], v[238:241], v[144:147], v[56:59]
	ds_read_b128 v[144:147], v79 offset:49152
	s_waitcnt lgkmcnt(1)
	v_mfma_f32_16x16x32_bf16 v[52:55], v[234:237], v[244:247], v[52:55]
	v_mfma_f32_16x16x32_bf16 v[48:51], v[238:241], v[244:247], v[48:51]
	ds_read_b128 v[244:247], v79 offset:57344
	s_waitcnt lgkmcnt(1)
	v_mfma_f32_16x16x32_bf16 v[44:47], v[234:237], v[144:147], v[44:47]
	v_mfma_f32_16x16x32_bf16 v[40:43], v[238:241], v[144:147], v[40:43]
	s_waitcnt lgkmcnt(0)
	v_mfma_f32_16x16x32_bf16 v[36:39], v[234:237], v[244:247], v[36:39]
	v_mfma_f32_16x16x32_bf16 v[32:35], v[238:241], v[244:247], v[32:35]
	v_add_u32_e32 v136, s0, v193
	v_readlane_b32 s16, v254, 16
	v_ashrrev_i32_e32 v137, 31, v136
	v_readlane_b32 s17, v254, 17
	v_mul_f32_e32 v0, 0x43800000, v0
	v_mul_f32_e32 v4, 0x43800000, v4
	v_lshl_add_u64 v[76:77], v[136:137], 2, s[16:17]
	global_load_dwordx4 v[72:75], v[76:77], off offset:16
	s_nop 0
	global_load_dwordx4 v[76:79], v[76:77], off
	v_mul_f32_e32 v1, 0x43800000, v1
	v_mul_f32_e32 v8, 0x43800000, v8
	v_mul_f32_e32 v12, 0x43800000, v12
	s_lshr_b32 s0, s61, 8
	s_and_b32 s0, s0, 8
	s_or_b32 s0, s0, s22
	s_lshl_b64 s[10:11], s[10:11], 12
	s_or_b32 s0, s10, s0
	s_mov_b32 s61, s1
	s_add_i32 s51, s51, 1
	v_add_u32_e32 v132, 0x100, v132
	v_add_u32_e32 v134, 0x100, v134
	s_cmp_eq_u32 s51, 4
	s_waitcnt vmcnt(1)
	v_pk_mul_f32 v[142:143], v[96:97], v[72:73]
	v_lshlrev_b64 v[96:97], 1, v[136:137]
	s_waitcnt vmcnt(0)
	v_pk_mul_f32 v[138:139], v[100:101], v[76:77]
	v_pk_mul_f32 v[140:141], v[98:99], v[74:75]
	v_cvt_pk_bf16_f32 v100, v142, v143
	v_lshl_add_u64 v[136:137], v[104:105], 0, v[96:97]
	v_cvt_pk_bf16_f32 v101, v140, v141
	v_pk_mul_f32 v[92:93], v[92:93], v[76:77]
	v_pk_mul_f32 v[102:103], v[102:103], v[78:79]
	v_cvt_pk_bf16_f32 v98, v138, v139
	v_pk_mul_f32 v[94:95], v[94:95], v[78:79]
	v_cvt_pk_bf16_f32 v99, v102, v103
	global_store_dwordx4 v[136:137], v[98:101], off offset:2048
	v_mov_b32_e32 v136, v141
	v_pk_mul_f32 v[84:85], v[84:85], v[76:77]
	v_mov_b32_e32 v100, v139
	v_mov_b32_e32 v101, v93
	v_pk_mul_f32 v[98:99], v[90:91], v[74:75]
	v_pk_mul_f32 v[90:91], v[88:89], v[72:73]
	v_mov_b32_e32 v88, v138
	v_mov_b32_e32 v89, v92
	v_pk_mul_f32 v[100:101], v[100:101], v[100:101]
	v_mov_b32_e32 v137, v99
	v_pk_fma_f32 v[88:89], v[88:89], v[88:89], v[100:101]
	v_mov_b32_e32 v100, v102
	v_mov_b32_e32 v102, v103
	v_mov_b32_e32 v103, v95
	v_mov_b32_e32 v101, v94
	v_pk_mul_f32 v[102:103], v[102:103], v[102:103]
	v_pk_mul_f32 v[136:137], v[136:137], v[136:137]
	v_pk_fma_f32 v[100:101], v[100:101], v[100:101], v[102:103]
	v_mov_b32_e32 v102, v143
	v_mov_b32_e32 v103, v91
	v_pk_add_f32 v[88:89], v[88:89], v[100:101]
	v_mov_b32_e32 v100, v142
	v_mov_b32_e32 v101, v90
	v_pk_mul_f32 v[102:103], v[102:103], v[102:103]
	v_cvt_pk_bf16_f32 v90, v90, v91
	v_cvt_pk_bf16_f32 v91, v98, v99
	v_pk_mul_f32 v[68:69], v[68:69], v[76:77]
	v_pk_fma_f32 v[100:101], v[100:101], v[100:101], v[102:103]
	v_mov_b32_e32 v102, v140
	v_mov_b32_e32 v103, v98
	v_pk_fma_f32 v[102:103], v[102:103], v[102:103], v[136:137]
	v_pk_mul_f32 v[86:87], v[86:87], v[78:79]
	v_pk_add_f32 v[100:101], v[100:101], v[102:103]
	v_pk_mul_f32 v[82:83], v[82:83], v[74:75]
	v_pk_add_f32 v[88:89], v[88:89], v[100:101]
	v_pk_mul_f32 v[80:81], v[80:81], v[72:73]
	v_pk_add_f32 v[130:131], v[130:131], v[88:89]
	v_cvt_pk_bf16_f32 v88, v92, v93
	v_lshl_add_u64 v[92:93], v[106:107], 0, v[96:97]
	v_cvt_pk_bf16_f32 v89, v94, v95
	global_store_dwordx4 v[92:93], v[88:91], off offset:2048
	v_lshl_add_u64 v[92:93], v[108:109], 0, v[96:97]
	v_pk_mul_f32 v[70:71], v[70:71], v[78:79]
	v_cvt_pk_bf16_f32 v88, v84, v85
	v_cvt_pk_bf16_f32 v89, v86, v87
	v_cvt_pk_bf16_f32 v90, v80, v81
	v_cvt_pk_bf16_f32 v91, v82, v83
	global_store_dwordx4 v[92:93], v[88:91], off offset:2048
	v_pk_mul_f32 v[64:65], v[64:65], v[72:73]
	v_pk_mul_f32 v[66:67], v[66:67], v[74:75]
	v_mov_b32_e32 v88, v84
	v_mov_b32_e32 v84, v85
	v_mov_b32_e32 v85, v69
	v_mov_b32_e32 v89, v68
	v_pk_mul_f32 v[84:85], v[84:85], v[84:85]
	v_cvt_pk_bf16_f32 v68, v68, v69
	v_cvt_pk_bf16_f32 v69, v70, v71
	v_pk_mul_f32 v[60:61], v[60:61], v[76:77]
	v_pk_fma_f32 v[84:85], v[88:89], v[88:89], v[84:85]
	v_mov_b32_e32 v88, v86
	v_mov_b32_e32 v86, v87
	v_mov_b32_e32 v87, v71
	v_mov_b32_e32 v89, v70
	v_pk_mul_f32 v[86:87], v[86:87], v[86:87]
	v_cvt_pk_bf16_f32 v70, v64, v65
	v_cvt_pk_bf16_f32 v71, v66, v67
	v_pk_mul_f32 v[52:53], v[52:53], v[76:77]
	v_pk_fma_f32 v[86:87], v[88:89], v[88:89], v[86:87]
	v_pk_mul_f32 v[62:63], v[62:63], v[78:79]
	v_pk_add_f32 v[84:85], v[84:85], v[86:87]
	v_mov_b32_e32 v86, v80
	v_mov_b32_e32 v80, v81
	v_mov_b32_e32 v81, v65
	v_mov_b32_e32 v87, v64
	v_pk_mul_f32 v[80:81], v[80:81], v[80:81]
	v_lshl_add_u64 v[64:65], v[110:111], 0, v[96:97]
	v_pk_fma_f32 v[80:81], v[86:87], v[86:87], v[80:81]
	v_mov_b32_e32 v86, v82
	v_mov_b32_e32 v87, v66
	v_mov_b32_e32 v82, v83
	v_mov_b32_e32 v83, v67
	global_store_dwordx4 v[64:65], v[68:71], off offset:2048
	v_pk_mul_f32 v[64:65], v[58:59], v[74:75]
	v_pk_mul_f32 v[66:67], v[56:57], v[72:73]
	v_cvt_pk_bf16_f32 v59, v64, v65
	v_lshl_add_u64 v[68:69], v[112:113], 0, v[96:97]
	v_cvt_pk_bf16_f32 v58, v66, v67
	v_cvt_pk_bf16_f32 v56, v60, v61
	v_cvt_pk_bf16_f32 v57, v62, v63
	global_store_dwordx4 v[68:69], v[56:59], off offset:2048
	v_pk_mul_f32 v[54:55], v[54:55], v[78:79]
	v_pk_mul_f32 v[44:45], v[44:45], v[76:77]
	v_mov_b32_e32 v58, v61
	v_mov_b32_e32 v59, v53
	v_pk_mul_f32 v[56:57], v[50:51], v[74:75]
	v_pk_mul_f32 v[50:51], v[48:49], v[72:73]
	v_mov_b32_e32 v48, v60
	v_mov_b32_e32 v49, v52
	v_pk_mul_f32 v[58:59], v[58:59], v[58:59]
	v_mov_b32_e32 v60, v63
	v_mov_b32_e32 v61, v55
	v_pk_fma_f32 v[48:49], v[48:49], v[48:49], v[58:59]
	v_mov_b32_e32 v58, v62
	v_mov_b32_e32 v59, v54
	v_pk_mul_f32 v[60:61], v[60:61], v[60:61]
	v_mov_b32_e32 v62, v65
	v_pk_fma_f32 v[58:59], v[58:59], v[58:59], v[60:61]
	v_mov_b32_e32 v60, v67
	v_mov_b32_e32 v61, v51
	v_pk_add_f32 v[48:49], v[48:49], v[58:59]
	v_mov_b32_e32 v58, v66
	v_mov_b32_e32 v59, v50
	v_pk_mul_f32 v[60:61], v[60:61], v[60:61]
	v_mov_b32_e32 v63, v57
	v_pk_fma_f32 v[58:59], v[58:59], v[58:59], v[60:61]
	v_mov_b32_e32 v60, v64
	v_mov_b32_e32 v61, v56
	v_pk_mul_f32 v[62:63], v[62:63], v[62:63]
	v_cvt_pk_bf16_f32 v50, v50, v51
	v_cvt_pk_bf16_f32 v51, v56, v57
	v_pk_mul_f32 v[36:37], v[36:37], v[76:77]
	v_pk_fma_f32 v[60:61], v[60:61], v[60:61], v[62:63]
	v_pk_mul_f32 v[46:47], v[46:47], v[78:79]
	v_pk_add_f32 v[58:59], v[58:59], v[60:61]
	v_pk_mul_f32 v[38:39], v[38:39], v[78:79]
	v_pk_add_f32 v[48:49], v[48:49], v[58:59]
	v_pk_mul_f32 v[82:83], v[82:83], v[82:83]
	v_pk_add_f32 v[126:127], v[126:127], v[48:49]
	v_cvt_pk_bf16_f32 v48, v52, v53
	v_cvt_pk_bf16_f32 v49, v54, v55
	v_lshl_add_u64 v[52:53], v[114:115], 0, v[96:97]
	global_store_dwordx4 v[52:53], v[48:51], off offset:2048
	v_lshl_add_u64 v[52:53], v[116:117], 0, v[96:97]
	v_pk_fma_f32 v[82:83], v[86:87], v[86:87], v[82:83]
	v_pk_mul_f32 v[48:49], v[42:43], v[74:75]
	v_pk_mul_f32 v[50:51], v[40:41], v[72:73]
	v_cvt_pk_bf16_f32 v43, v48, v49
	v_cvt_pk_bf16_f32 v40, v44, v45
	v_cvt_pk_bf16_f32 v41, v46, v47
	v_pk_add_f32 v[80:81], v[80:81], v[82:83]
	v_cvt_pk_bf16_f32 v42, v50, v51
	global_store_dwordx4 v[52:53], v[40:43], off offset:2048
	v_pk_add_f32 v[80:81], v[84:85], v[80:81]
	s_nop 0
	v_mov_b32_e32 v42, v45
	v_mov_b32_e32 v43, v37
	v_pk_mul_f32 v[40:41], v[34:35], v[74:75]
	v_pk_mul_f32 v[34:35], v[32:33], v[72:73]
	v_mov_b32_e32 v32, v44
	v_mov_b32_e32 v33, v36
	v_pk_mul_f32 v[42:43], v[42:43], v[42:43]
	v_mov_b32_e32 v44, v47
	v_mov_b32_e32 v45, v39
	v_pk_fma_f32 v[32:33], v[32:33], v[32:33], v[42:43]
	v_mov_b32_e32 v42, v46
	v_mov_b32_e32 v43, v38
	v_pk_mul_f32 v[44:45], v[44:45], v[44:45]
	v_mov_b32_e32 v46, v49
	v_pk_fma_f32 v[42:43], v[42:43], v[42:43], v[44:45]
	v_mov_b32_e32 v44, v51
	v_mov_b32_e32 v45, v35
	v_pk_add_f32 v[32:33], v[32:33], v[42:43]
	v_mov_b32_e32 v42, v50
	v_mov_b32_e32 v43, v34
	v_pk_mul_f32 v[44:45], v[44:45], v[44:45]
	v_mov_b32_e32 v47, v41
	v_pk_fma_f32 v[42:43], v[42:43], v[42:43], v[44:45]
	v_mov_b32_e32 v44, v48
	v_mov_b32_e32 v45, v40
	v_pk_mul_f32 v[46:47], v[46:47], v[46:47]
	v_cvt_pk_bf16_f32 v34, v34, v35
	v_cvt_pk_bf16_f32 v35, v40, v41
	v_pk_add_f32 v[128:129], v[128:129], v[80:81]
	v_pk_fma_f32 v[44:45], v[44:45], v[44:45], v[46:47]
	s_nop 0
	v_pk_add_f32 v[42:43], v[42:43], v[44:45]
	s_nop 0
	v_pk_add_f32 v[32:33], v[32:33], v[42:43]
	s_nop 0
	v_pk_add_f32 v[122:123], v[122:123], v[32:33]
	v_cvt_pk_bf16_f32 v32, v36, v37
	v_lshl_add_u64 v[36:37], v[118:119], 0, v[96:97]
	v_cvt_pk_bf16_f32 v33, v38, v39
	global_store_dwordx4 v[36:37], v[32:35], off offset:2048
	s_nop 1
	v_mov_b32_e32 v34, v157
	v_cvt_pk_fp8_f32 v34, v0, v4
	v_mul_f32_e32 v0, 0x43800000, v16
	v_mul_f32_e32 v4, 0x43800000, v20
	v_mov_b32_e32 v35, v157
	v_cvt_pk_fp8_f32 v35, v0, v4
	v_mul_f32_e32 v4, 0x43800000, v5
	v_mov_b32_e32 v0, v157
	v_cvt_pk_fp8_f32 v0, v1, v4
	v_cvt_pk_fp8_f32 v34, v8, v12 op_sel:[0,0,1]
	v_mul_f32_e32 v8, 0x43800000, v24
	v_mul_f32_e32 v12, 0x43800000, v28
	v_cvt_pk_fp8_f32 v35, v8, v12 op_sel:[0,0,1]
	v_mul_f32_e32 v5, 0x43800000, v9
	v_mul_f32_e32 v8, 0x43800000, v13
	v_cvt_pk_fp8_f32 v0, v5, v8 op_sel:[0,0,1]
	v_mul_f32_e32 v4, 0x43800000, v17
	v_mul_f32_e32 v5, 0x43800000, v21
	v_mov_b32_e32 v1, v157
	v_cvt_pk_fp8_f32 v1, v4, v5
	v_mov_b32_e32 v33, s11
	v_or_b32_e32 v32, s0, v162
	v_mul_f32_e32 v8, 0x43800000, v25
	v_mul_f32_e32 v9, 0x43800000, v29
	v_lshlrev_b64 v[32:33], 11, v[32:33]
	v_cvt_pk_fp8_f32 v1, v8, v9 op_sel:[0,0,1]
	v_lshl_add_u64 v[32:33], s[86:87], 0, v[32:33]
	v_lshl_add_u64 v[32:33], v[32:33], 0, s[60:61]
	v_lshl_add_u64 v[32:33], v[32:33], 0, v[160:161]
	global_store_dwordx2 v[32:33], v[0:1], off offset:2048
	v_mul_f32_e32 v1, 0x43800000, v2
	v_mul_f32_e32 v2, 0x43800000, v6
	v_mov_b32_e32 v0, v157
	v_cvt_pk_fp8_f32 v0, v1, v2
	v_mul_f32_e32 v4, 0x43800000, v10
	v_mul_f32_e32 v5, 0x43800000, v14
	v_mul_f32_e32 v2, 0x43800000, v18
	v_cvt_pk_fp8_f32 v0, v4, v5 op_sel:[0,0,1]
	v_mul_f32_e32 v4, 0x43800000, v22
	v_mov_b32_e32 v1, v157
	v_cvt_pk_fp8_f32 v1, v2, v4
	v_mul_f32_e32 v5, 0x43800000, v26
	v_mul_f32_e32 v6, 0x43800000, v30
	v_add_co_u32_e32 v4, vcc, s18, v32
	v_cvt_pk_fp8_f32 v1, v5, v6 op_sel:[0,0,1]
	s_nop 0
	v_addc_co_u32_e32 v5, vcc, 0, v33, vcc
	v_mul_f32_e32 v2, 0x43800000, v7
	global_store_dwordx2 v[4:5], v[0:1], off
	v_mul_f32_e32 v1, 0x43800000, v3
	v_mov_b32_e32 v0, v157
	v_cvt_pk_fp8_f32 v0, v1, v2
	v_mul_f32_e32 v3, 0x43800000, v11
	v_mul_f32_e32 v6, 0x43800000, v15
	v_mul_f32_e32 v2, 0x43800000, v19
	v_cvt_pk_fp8_f32 v0, v3, v6 op_sel:[0,0,1]
	v_mul_f32_e32 v3, 0x43800000, v23
	v_mov_b32_e32 v1, v157
	v_cvt_pk_fp8_f32 v1, v2, v3
	v_mul_f32_e32 v6, 0x43800000, v27
	v_mul_f32_e32 v7, 0x43800000, v31
	global_store_dwordx2 v[32:33], v[34:35], off
	v_cvt_pk_fp8_f32 v1, v6, v7 op_sel:[0,0,1]
	global_store_dwordx2 v[4:5], v[0:1], off offset:2048
	s_cbranch_scc0 .LBB0_378
	ds_bpermute_b32 v0, v174, v130
	v_readlane_b32 s0, v254, 18
	v_readlane_b32 s8, v255, 51
	v_readlane_b32 s9, v255, 52
	s_waitcnt lgkmcnt(0)
	v_add_f32_e32 v1, v130, v0
	ds_bpermute_b32 v2, v175, v1
	v_lshlrev_b32_e32 v0, 5, v202
	v_add_u32_e32 v0, s0, v0
	s_and_saveexec_b64 s[2:3], s[8:9]
	s_cbranch_execz .LBB0_543
	s_waitcnt lgkmcnt(0)
	v_add_f32_e32 v1, v1, v2
	ds_write_b32 v0, v1

.LBB0_1014:
	s_bitcmp1_b32 s60, 0
	s_cselect_b32 s29, 0xc00, 0
	s_lshl_b32 s38, s56, 2
	s_or_b32 s38, s29, s38
	v_mbcnt_lo_u32_b32 v133, -1, 0
	v_mbcnt_hi_u32_b32 v133, -1, v133
	s_add_i32 s38, s38, 0x24c00
	v_and_b32_e32 v135, -16, v133
	v_lshl_add_u32 v131, v135, 2, s38
	s_or_b32 s38, s29, 0x25000
	s_add_i32 s39, s29, 0x25400
	s_lshl_b32 s29, s0, 8
	v_readlane_b32 s36, v254, 13
	s_or_b32 s29, s29, s56
	v_readlane_b32 s37, v254, 14
	v_add_u32_e32 v140, s29, v135
	s_lshl_b32 s29, s4, 2
	s_add_i32 s29, s29, 0x248a0
	s_mov_b64 s[36:37], s[100:101]
	v_mov_b32_e32 v135, s29
	ds_read_b32 v135, v135
	v_and_or_b32 v178, v133, 15, s52
	v_ashrrev_i32_e32 v141, 31, v140
	s_lshl_b32 s29, s47, 8
	s_waitcnt lgkmcnt(0)
	v_lshl_add_u64 v[140:141], s[36:37], 0, v[140:141]
	v_add_u32_e32 v139, s29, v178
	v_lshlrev_b32_e32 v137, 2, v178
	v_lshl_add_u64 v[140:141], v[140:141], 0, s[22:23]
	v_cmp_lt_i32_e32 vcc, v139, v135
	v_add_u32_e32 v133, s38, v137
	v_add_u32_e32 v137, s39, v137
	ds_read_b128 v[182:185], v131
	ds_read_b128 v[186:189], v131 offset:16
	ds_read_b128 v[190:193], v131 offset:32
	ds_read_b128 v[194:197], v131 offset:48
	ds_read_b32 v198, v137
	ds_read_b32 v199, v133
	ds_read_b32 v200, v137 offset:64
	ds_read_b32 v201, v133 offset:64
	ds_read_b32 v202, v137 offset:128
	ds_read_b32 v203, v133 offset:128
	ds_read_b32 v204, v137 offset:192
	ds_read_b32 v205, v133 offset:192
	ds_read_b32 v206, v137 offset:512
	ds_read_b32 v207, v133 offset:512
	ds_read_b32 v208, v137 offset:576
	ds_read_b32 v209, v133 offset:576
	ds_read_b32 v210, v137 offset:640
	ds_read_b32 v211, v133 offset:640
	ds_read_b32 v212, v137 offset:704
	ds_read_b32 v213, v133 offset:704
	s_waitcnt lgkmcnt(0)
	s_and_saveexec_b64 s[36:37], vcc
	s_cbranch_execz .LBB0_1016
	v_mov_b32_e32 v160, v199
	v_mul_f32_e32 v162, 0x41000000, v198
	v_pk_fma_f32 v[144:145], v[100:101], s[24:25], v[182:183] op_sel_hi:[1,0,1]
	v_pk_fma_f32 v[146:147], v[102:103], s[24:25], v[184:185] op_sel_hi:[1,0,1]
	v_pk_mul_f32 v[180:181], v[144:145], v[162:163] op_sel_hi:[1,0]
	v_pk_fma_f32 v[144:145], v[96:97], s[24:25], v[186:187] op_sel_hi:[1,0,1]
	v_pk_mul_f32 v[146:147], v[146:147], v[162:163] op_sel_hi:[1,0]
	v_pk_mul_f32 v[148:149], v[162:163], v[144:145] op_sel_hi:[0,1]
	v_mov_b32_e32 v144, v129
	v_cvt_pk_fp8_f32 v144, v180, v181
	v_mov_b32_e32 v145, v129
	v_cvt_pk_fp8_f32 v145, v148, v149
	v_pk_fma_f32 v[148:149], v[98:99], s[24:25], v[188:189] op_sel_hi:[1,0,1]
	v_cvt_pk_fp8_f32 v144, v146, v147 op_sel:[0,0,1]
	v_pk_mul_f32 v[148:149], v[162:163], v[148:149] op_sel_hi:[0,1]
	v_pk_fma_f32 v[146:147], v[70:71], s[24:25], v[192:193] op_sel_hi:[1,0,1]
	v_cvt_pk_fp8_f32 v145, v148, v149 op_sel:[0,0,1]
	v_pk_fma_f32 v[148:149], v[68:69], s[24:25], v[190:191] op_sel_hi:[1,0,1]
	v_pk_mul_f32 v[150:151], v[162:163], v[146:147] op_sel_hi:[0,1]
	v_pk_fma_f32 v[146:147], v[64:65], s[24:25], v[194:195] op_sel_hi:[1,0,1]
	v_pk_mul_f32 v[148:149], v[162:163], v[148:149] op_sel_hi:[0,1]
	v_pk_mul_f32 v[152:153], v[162:163], v[146:147] op_sel_hi:[0,1]
	v_mov_b32_e32 v146, v129
	v_mov_b32_e32 v147, v129
	v_cvt_pk_fp8_f32 v146, v148, v149
	v_cvt_pk_fp8_f32 v147, v152, v153
	v_pk_fma_f32 v[148:149], v[66:67], s[24:25], v[196:197] op_sel_hi:[1,0,1]
	v_ashrrev_i32_e32 v161, 31, v160
	v_pk_mul_f32 v[148:149], v[162:163], v[148:149] op_sel_hi:[0,1]
	v_cvt_pk_fp8_f32 v146, v150, v151 op_sel:[0,0,1]
	v_cvt_pk_fp8_f32 v147, v148, v149 op_sel:[0,0,1]
	v_lshlrev_b64 v[148:149], 11, v[160:161]
	v_lshl_add_u64 v[148:149], v[140:141], 0, v[148:149]
	global_store_dwordx4 v[148:149], v[144:147], off
.LBB0_1016:
	s_or_b64 exec, exec, s[36:37]
	s_nop 0
	v_add3_u32 v144, s29, v178, 16
	v_cmp_lt_i32_e32 vcc, v144, v135
	s_and_saveexec_b64 s[36:37], vcc
	s_cbranch_execz .LBB0_1018
	v_mov_b32_e32 v160, v201
	v_mul_f32_e32 v162, 0x41000000, v200
	v_pk_fma_f32 v[144:145], v[92:93], s[24:25], v[182:183] op_sel_hi:[1,0,1]
	v_pk_fma_f32 v[146:147], v[94:95], s[24:25], v[184:185] op_sel_hi:[1,0,1]
	v_pk_mul_f32 v[180:181], v[144:145], v[162:163] op_sel_hi:[1,0]
	v_pk_fma_f32 v[144:145], v[88:89], s[24:25], v[186:187] op_sel_hi:[1,0,1]
	v_pk_mul_f32 v[146:147], v[146:147], v[162:163] op_sel_hi:[1,0]
	v_pk_mul_f32 v[148:149], v[162:163], v[144:145] op_sel_hi:[0,1]
	v_mov_b32_e32 v144, v129
	v_cvt_pk_fp8_f32 v144, v180, v181
	v_mov_b32_e32 v145, v129
	v_cvt_pk_fp8_f32 v145, v148, v149
	v_pk_fma_f32 v[148:149], v[90:91], s[24:25], v[188:189] op_sel_hi:[1,0,1]
	v_cvt_pk_fp8_f32 v144, v146, v147 op_sel:[0,0,1]
	v_pk_mul_f32 v[148:149], v[162:163], v[148:149] op_sel_hi:[0,1]
	v_pk_fma_f32 v[146:147], v[62:63], s[24:25], v[192:193] op_sel_hi:[1,0,1]
	v_cvt_pk_fp8_f32 v145, v148, v149 op_sel:[0,0,1]
	v_pk_fma_f32 v[148:149], v[60:61], s[24:25], v[190:191] op_sel_hi:[1,0,1]
	v_pk_mul_f32 v[150:151], v[162:163], v[146:147] op_sel_hi:[0,1]
	v_pk_fma_f32 v[146:147], v[56:57], s[24:25], v[194:195] op_sel_hi:[1,0,1]
	v_pk_mul_f32 v[148:149], v[162:163], v[148:149] op_sel_hi:[0,1]
	v_pk_mul_f32 v[152:153], v[162:163], v[146:147] op_sel_hi:[0,1]
	v_mov_b32_e32 v146, v129
	v_mov_b32_e32 v147, v129
	v_cvt_pk_fp8_f32 v146, v148, v149
	v_cvt_pk_fp8_f32 v147, v152, v153
	v_pk_fma_f32 v[148:149], v[58:59], s[24:25], v[196:197] op_sel_hi:[1,0,1]
	v_ashrrev_i32_e32 v161, 31, v160
	v_pk_mul_f32 v[148:149], v[162:163], v[148:149] op_sel_hi:[0,1]
	v_cvt_pk_fp8_f32 v146, v150, v151 op_sel:[0,0,1]
	v_cvt_pk_fp8_f32 v147, v148, v149 op_sel:[0,0,1]
	v_lshlrev_b64 v[148:149], 11, v[160:161]
	v_lshl_add_u64 v[148:149], v[140:141], 0, v[148:149]
	global_store_dwordx4 v[148:149], v[144:147], off
.LBB0_1018:
	s_or_b64 exec, exec, s[36:37]
	s_nop 0
	v_add3_u32 v144, s29, v178, 32
	v_cmp_lt_i32_e32 vcc, v144, v135
	s_and_saveexec_b64 s[36:37], vcc
	s_cbranch_execz .LBB0_1020
	v_mov_b32_e32 v160, v203
	v_mul_f32_e32 v162, 0x41000000, v202
	v_pk_fma_f32 v[144:145], v[84:85], s[24:25], v[182:183] op_sel_hi:[1,0,1]
	v_pk_fma_f32 v[146:147], v[86:87], s[24:25], v[184:185] op_sel_hi:[1,0,1]
	v_pk_mul_f32 v[180:181], v[144:145], v[162:163] op_sel_hi:[1,0]
	v_pk_fma_f32 v[144:145], v[80:81], s[24:25], v[186:187] op_sel_hi:[1,0,1]
	v_pk_mul_f32 v[146:147], v[146:147], v[162:163] op_sel_hi:[1,0]
	v_pk_mul_f32 v[148:149], v[162:163], v[144:145] op_sel_hi:[0,1]
	v_mov_b32_e32 v144, v129
	v_cvt_pk_fp8_f32 v144, v180, v181
	v_mov_b32_e32 v145, v129
	v_cvt_pk_fp8_f32 v145, v148, v149
	v_pk_fma_f32 v[148:149], v[82:83], s[24:25], v[188:189] op_sel_hi:[1,0,1]
	v_cvt_pk_fp8_f32 v144, v146, v147 op_sel:[0,0,1]
	v_pk_mul_f32 v[148:149], v[162:163], v[148:149] op_sel_hi:[0,1]
	v_pk_fma_f32 v[146:147], v[54:55], s[24:25], v[192:193] op_sel_hi:[1,0,1]
	v_cvt_pk_fp8_f32 v145, v148, v149 op_sel:[0,0,1]
	v_pk_fma_f32 v[148:149], v[52:53], s[24:25], v[190:191] op_sel_hi:[1,0,1]
	v_pk_mul_f32 v[150:151], v[162:163], v[146:147] op_sel_hi:[0,1]
	v_pk_fma_f32 v[146:147], v[48:49], s[24:25], v[194:195] op_sel_hi:[1,0,1]
	v_pk_mul_f32 v[148:149], v[162:163], v[148:149] op_sel_hi:[0,1]
	v_pk_mul_f32 v[152:153], v[162:163], v[146:147] op_sel_hi:[0,1]
	v_mov_b32_e32 v146, v129
	v_mov_b32_e32 v147, v129
	v_cvt_pk_fp8_f32 v146, v148, v149
	v_cvt_pk_fp8_f32 v147, v152, v153
	v_pk_fma_f32 v[148:149], v[50:51], s[24:25], v[196:197] op_sel_hi:[1,0,1]
	v_ashrrev_i32_e32 v161, 31, v160
	v_pk_mul_f32 v[148:149], v[162:163], v[148:149] op_sel_hi:[0,1]
	v_cvt_pk_fp8_f32 v146, v150, v151 op_sel:[0,0,1]
	v_cvt_pk_fp8_f32 v147, v148, v149 op_sel:[0,0,1]
	v_lshlrev_b64 v[148:149], 11, v[160:161]
	v_lshl_add_u64 v[148:149], v[140:141], 0, v[148:149]
	global_store_dwordx4 v[148:149], v[144:147], off
.LBB0_1020:
	s_or_b64 exec, exec, s[36:37]
	s_nop 0
	v_add3_u32 v144, s29, v178, 48
	v_cmp_lt_i32_e32 vcc, v144, v135
	s_and_saveexec_b64 s[36:37], vcc
	s_cbranch_execz .LBB0_1022
	v_mov_b32_e32 v160, v205
	v_mul_f32_e32 v162, 0x41000000, v204
	v_pk_fma_f32 v[144:145], v[76:77], s[24:25], v[182:183] op_sel_hi:[1,0,1]
	v_pk_fma_f32 v[146:147], v[78:79], s[24:25], v[184:185] op_sel_hi:[1,0,1]
	v_pk_mul_f32 v[178:179], v[144:145], v[162:163] op_sel_hi:[1,0]
	v_pk_fma_f32 v[144:145], v[72:73], s[24:25], v[186:187] op_sel_hi:[1,0,1]
	v_pk_mul_f32 v[146:147], v[146:147], v[162:163] op_sel_hi:[1,0]
	v_pk_mul_f32 v[148:149], v[162:163], v[144:145] op_sel_hi:[0,1]
	v_mov_b32_e32 v144, v129
	v_cvt_pk_fp8_f32 v144, v178, v179
	v_mov_b32_e32 v145, v129
	v_cvt_pk_fp8_f32 v145, v148, v149
	v_pk_fma_f32 v[148:149], v[74:75], s[24:25], v[188:189] op_sel_hi:[1,0,1]
	v_cvt_pk_fp8_f32 v144, v146, v147 op_sel:[0,0,1]
	v_pk_mul_f32 v[148:149], v[162:163], v[148:149] op_sel_hi:[0,1]
	v_pk_fma_f32 v[146:147], v[42:43], s[24:25], v[192:193] op_sel_hi:[1,0,1]
	v_cvt_pk_fp8_f32 v145, v148, v149 op_sel:[0,0,1]
	v_pk_fma_f32 v[148:149], v[40:41], s[24:25], v[190:191] op_sel_hi:[1,0,1]
	v_pk_mul_f32 v[150:151], v[162:163], v[146:147] op_sel_hi:[0,1]
	v_pk_fma_f32 v[146:147], v[32:33], s[24:25], v[194:195] op_sel_hi:[1,0,1]
	v_pk_mul_f32 v[148:149], v[162:163], v[148:149] op_sel_hi:[0,1]
	v_pk_mul_f32 v[152:153], v[162:163], v[146:147] op_sel_hi:[0,1]
	v_mov_b32_e32 v146, v129
	v_mov_b32_e32 v147, v129
	v_cvt_pk_fp8_f32 v146, v148, v149
	v_cvt_pk_fp8_f32 v147, v152, v153
	v_pk_fma_f32 v[148:149], v[34:35], s[24:25], v[196:197] op_sel_hi:[1,0,1]
	v_ashrrev_i32_e32 v161, 31, v160
	v_pk_mul_f32 v[148:149], v[162:163], v[148:149] op_sel_hi:[0,1]
	v_cvt_pk_fp8_f32 v146, v150, v151 op_sel:[0,0,1]
	v_cvt_pk_fp8_f32 v147, v148, v149 op_sel:[0,0,1]
	v_lshlrev_b64 v[148:149], 11, v[160:161]
	v_lshl_add_u64 v[148:149], v[140:141], 0, v[148:149]
	global_store_dwordx4 v[148:149], v[144:147], off
.LBB0_1022:
	s_or_b64 exec, exec, s[36:37]
	s_nop 0
	v_add_u32_e32 v144, 0x80, v139
	v_cmp_lt_i32_e32 vcc, v144, v135
	s_and_saveexec_b64 s[36:37], vcc
	s_cbranch_execz .LBB0_1024
	v_mov_b32_e32 v160, v207
	v_mul_f32_e32 v162, 0x41000000, v206
	v_pk_fma_f32 v[144:145], v[44:45], s[24:25], v[182:183] op_sel_hi:[1,0,1]
	v_pk_fma_f32 v[146:147], v[46:47], s[24:25], v[184:185] op_sel_hi:[1,0,1]
	v_pk_mul_f32 v[178:179], v[144:145], v[162:163] op_sel_hi:[1,0]
	v_pk_fma_f32 v[144:145], v[36:37], s[24:25], v[186:187] op_sel_hi:[1,0,1]
	v_pk_mul_f32 v[146:147], v[146:147], v[162:163] op_sel_hi:[1,0]
	v_pk_mul_f32 v[148:149], v[162:163], v[144:145] op_sel_hi:[0,1]
	v_mov_b32_e32 v144, v129
	v_cvt_pk_fp8_f32 v144, v178, v179
	v_mov_b32_e32 v145, v129
	v_cvt_pk_fp8_f32 v145, v148, v149
	v_pk_fma_f32 v[148:149], v[38:39], s[24:25], v[188:189] op_sel_hi:[1,0,1]
	v_cvt_pk_fp8_f32 v144, v146, v147 op_sel:[0,0,1]
	v_pk_mul_f32 v[148:149], v[162:163], v[148:149] op_sel_hi:[0,1]
	v_pk_fma_f32 v[146:147], v[6:7], s[24:25], v[192:193] op_sel_hi:[1,0,1]
	v_cvt_pk_fp8_f32 v145, v148, v149 op_sel:[0,0,1]
	v_pk_fma_f32 v[148:149], v[4:5], s[24:25], v[190:191] op_sel_hi:[1,0,1]
	v_pk_mul_f32 v[150:151], v[162:163], v[146:147] op_sel_hi:[0,1]
	v_pk_fma_f32 v[146:147], v[0:1], s[24:25], v[194:195] op_sel_hi:[1,0,1]
	v_pk_mul_f32 v[148:149], v[162:163], v[148:149] op_sel_hi:[0,1]
	v_pk_mul_f32 v[152:153], v[162:163], v[146:147] op_sel_hi:[0,1]
	v_mov_b32_e32 v146, v129
	v_mov_b32_e32 v147, v129
	v_cvt_pk_fp8_f32 v146, v148, v149
	v_cvt_pk_fp8_f32 v147, v152, v153
	v_pk_fma_f32 v[148:149], v[2:3], s[24:25], v[196:197] op_sel_hi:[1,0,1]
	v_ashrrev_i32_e32 v161, 31, v160
	v_pk_mul_f32 v[148:149], v[162:163], v[148:149] op_sel_hi:[0,1]
	v_cvt_pk_fp8_f32 v146, v150, v151 op_sel:[0,0,1]
	v_cvt_pk_fp8_f32 v147, v148, v149 op_sel:[0,0,1]
	v_lshlrev_b64 v[148:149], 11, v[160:161]
	v_lshl_add_u64 v[148:149], v[140:141], 0, v[148:149]
	global_store_dwordx4 v[148:149], v[144:147], off
.LBB0_1024:
	s_or_b64 exec, exec, s[36:37]
	s_nop 0
	v_add_u32_e32 v144, 0x90, v139
	v_cmp_lt_i32_e32 vcc, v144, v135
	s_and_saveexec_b64 s[36:37], vcc
	s_cbranch_execz .LBB0_1026
	v_mov_b32_e32 v160, v209
	v_mul_f32_e32 v162, 0x41000000, v208
	v_pk_fma_f32 v[144:145], v[28:29], s[24:25], v[182:183] op_sel_hi:[1,0,1]
	v_pk_fma_f32 v[146:147], v[30:31], s[24:25], v[184:185] op_sel_hi:[1,0,1]
	v_pk_mul_f32 v[178:179], v[144:145], v[162:163] op_sel_hi:[1,0]
	v_pk_fma_f32 v[144:145], v[24:25], s[24:25], v[186:187] op_sel_hi:[1,0,1]
	v_pk_mul_f32 v[146:147], v[146:147], v[162:163] op_sel_hi:[1,0]
	v_pk_mul_f32 v[148:149], v[162:163], v[144:145] op_sel_hi:[0,1]
	v_mov_b32_e32 v144, v129
	v_cvt_pk_fp8_f32 v144, v178, v179
	v_mov_b32_e32 v145, v129
	v_cvt_pk_fp8_f32 v145, v148, v149
	v_pk_fma_f32 v[148:149], v[26:27], s[24:25], v[188:189] op_sel_hi:[1,0,1]
	v_cvt_pk_fp8_f32 v144, v146, v147 op_sel:[0,0,1]
	v_pk_mul_f32 v[148:149], v[162:163], v[148:149] op_sel_hi:[0,1]
	v_pk_fma_f32 v[146:147], v[106:107], s[24:25], v[192:193] op_sel_hi:[1,0,1]
	v_cvt_pk_fp8_f32 v145, v148, v149 op_sel:[0,0,1]
	v_pk_fma_f32 v[148:149], v[104:105], s[24:25], v[190:191] op_sel_hi:[1,0,1]
	v_pk_mul_f32 v[150:151], v[162:163], v[146:147] op_sel_hi:[0,1]
	v_pk_fma_f32 v[146:147], v[108:109], s[24:25], v[194:195] op_sel_hi:[1,0,1]
	v_pk_mul_f32 v[148:149], v[162:163], v[148:149] op_sel_hi:[0,1]
	v_pk_mul_f32 v[152:153], v[162:163], v[146:147] op_sel_hi:[0,1]
	v_mov_b32_e32 v146, v129
	v_mov_b32_e32 v147, v129
	v_cvt_pk_fp8_f32 v146, v148, v149
	v_cvt_pk_fp8_f32 v147, v152, v153
	v_pk_fma_f32 v[148:149], v[110:111], s[24:25], v[196:197] op_sel_hi:[1,0,1]
	v_ashrrev_i32_e32 v161, 31, v160
	v_pk_mul_f32 v[148:149], v[162:163], v[148:149] op_sel_hi:[0,1]
	v_cvt_pk_fp8_f32 v146, v150, v151 op_sel:[0,0,1]
	v_cvt_pk_fp8_f32 v147, v148, v149 op_sel:[0,0,1]
	v_lshlrev_b64 v[148:149], 11, v[160:161]
	v_lshl_add_u64 v[148:149], v[140:141], 0, v[148:149]
	global_store_dwordx4 v[148:149], v[144:147], off
.LBB0_1026:
	s_or_b64 exec, exec, s[36:37]
	s_nop 0
	v_add_u32_e32 v144, 0xa0, v139
	v_cmp_lt_i32_e32 vcc, v144, v135
	s_and_saveexec_b64 s[36:37], vcc
	s_cbranch_execz .LBB0_1028
	v_mov_b32_e32 v160, v211
	v_mul_f32_e32 v162, 0x41000000, v210
	v_pk_fma_f32 v[144:145], v[20:21], s[24:25], v[182:183] op_sel_hi:[1,0,1]
	v_pk_fma_f32 v[146:147], v[22:23], s[24:25], v[184:185] op_sel_hi:[1,0,1]
	v_pk_mul_f32 v[178:179], v[144:145], v[162:163] op_sel_hi:[1,0]
	v_pk_fma_f32 v[144:145], v[16:17], s[24:25], v[186:187] op_sel_hi:[1,0,1]
	v_pk_mul_f32 v[146:147], v[146:147], v[162:163] op_sel_hi:[1,0]
	v_pk_mul_f32 v[148:149], v[162:163], v[144:145] op_sel_hi:[0,1]
	v_mov_b32_e32 v144, v129
	v_cvt_pk_fp8_f32 v144, v178, v179
	v_mov_b32_e32 v145, v129
	v_cvt_pk_fp8_f32 v145, v148, v149
	v_pk_fma_f32 v[148:149], v[18:19], s[24:25], v[188:189] op_sel_hi:[1,0,1]
	v_cvt_pk_fp8_f32 v144, v146, v147 op_sel:[0,0,1]
	v_pk_mul_f32 v[148:149], v[162:163], v[148:149] op_sel_hi:[0,1]
	v_pk_fma_f32 v[146:147], v[114:115], s[24:25], v[192:193] op_sel_hi:[1,0,1]
	v_cvt_pk_fp8_f32 v145, v148, v149 op_sel:[0,0,1]
	v_pk_fma_f32 v[148:149], v[112:113], s[24:25], v[190:191] op_sel_hi:[1,0,1]
	v_pk_mul_f32 v[150:151], v[162:163], v[146:147] op_sel_hi:[0,1]
	v_pk_fma_f32 v[146:147], v[116:117], s[24:25], v[194:195] op_sel_hi:[1,0,1]
	v_pk_mul_f32 v[148:149], v[162:163], v[148:149] op_sel_hi:[0,1]
	v_pk_mul_f32 v[152:153], v[162:163], v[146:147] op_sel_hi:[0,1]
	v_mov_b32_e32 v146, v129
	v_mov_b32_e32 v147, v129
	v_cvt_pk_fp8_f32 v146, v148, v149
	v_cvt_pk_fp8_f32 v147, v152, v153
	v_pk_fma_f32 v[148:149], v[118:119], s[24:25], v[196:197] op_sel_hi:[1,0,1]
	v_ashrrev_i32_e32 v161, 31, v160
	v_pk_mul_f32 v[148:149], v[162:163], v[148:149] op_sel_hi:[0,1]
	v_cvt_pk_fp8_f32 v146, v150, v151 op_sel:[0,0,1]
	v_cvt_pk_fp8_f32 v147, v148, v149 op_sel:[0,0,1]
	v_lshlrev_b64 v[148:149], 11, v[160:161]
	v_lshl_add_u64 v[148:149], v[140:141], 0, v[148:149]
	global_store_dwordx4 v[148:149], v[144:147], off
.LBB0_1028:
	s_or_b64 exec, exec, s[36:37]
	v_add_u32_e32 v139, 0xb0, v139
	v_cmp_lt_i32_e32 vcc, v139, v135
	s_and_saveexec_b64 s[36:37], vcc
	s_cbranch_execz .LBB0_1030
	v_mov_b32_e32 v160, v213
	v_mul_f32_e32 v162, 0x41000000, v212
	v_ashrrev_i32_e32 v161, 31, v160
	v_pk_fma_f32 v[144:145], v[12:13], s[24:25], v[182:183] op_sel_hi:[1,0,1]
	v_pk_fma_f32 v[146:147], v[14:15], s[24:25], v[184:185] op_sel_hi:[1,0,1]
	v_pk_mul_f32 v[178:179], v[144:145], v[162:163] op_sel_hi:[1,0]
	v_pk_fma_f32 v[144:145], v[8:9], s[24:25], v[186:187] op_sel_hi:[1,0,1]
	v_pk_mul_f32 v[146:147], v[146:147], v[162:163] op_sel_hi:[1,0]
	v_pk_mul_f32 v[148:149], v[162:163], v[144:145] op_sel_hi:[0,1]
	v_mov_b32_e32 v144, v129
	v_cvt_pk_fp8_f32 v144, v178, v179
	v_mov_b32_e32 v145, v129
	v_cvt_pk_fp8_f32 v145, v148, v149
	v_pk_fma_f32 v[148:149], v[10:11], s[24:25], v[188:189] op_sel_hi:[1,0,1]
	v_cvt_pk_fp8_f32 v144, v146, v147 op_sel:[0,0,1]
	v_pk_mul_f32 v[148:149], v[162:163], v[148:149] op_sel_hi:[0,1]
	v_pk_fma_f32 v[146:147], v[122:123], s[24:25], v[192:193] op_sel_hi:[1,0,1]
	v_cvt_pk_fp8_f32 v145, v148, v149 op_sel:[0,0,1]
	v_pk_fma_f32 v[148:149], v[120:121], s[24:25], v[190:191] op_sel_hi:[1,0,1]
	v_pk_mul_f32 v[150:151], v[162:163], v[146:147] op_sel_hi:[0,1]
	v_pk_fma_f32 v[146:147], v[124:125], s[24:25], v[194:195] op_sel_hi:[1,0,1]
	v_pk_mul_f32 v[148:149], v[162:163], v[148:149] op_sel_hi:[0,1]
	v_pk_mul_f32 v[152:153], v[162:163], v[146:147] op_sel_hi:[0,1]
	v_mov_b32_e32 v146, v129
	v_mov_b32_e32 v147, v129
	v_cvt_pk_fp8_f32 v146, v148, v149
	v_cvt_pk_fp8_f32 v147, v152, v153
	v_pk_fma_f32 v[148:149], v[126:127], s[24:25], v[196:197] op_sel_hi:[1,0,1]
	v_cvt_pk_fp8_f32 v146, v150, v151 op_sel:[0,0,1]
	v_pk_mul_f32 v[148:149], v[162:163], v[148:149] op_sel_hi:[0,1]
	v_cvt_pk_fp8_f32 v147, v148, v149 op_sel:[0,0,1]
	v_lshlrev_b64 v[148:149], 11, v[160:161]
	v_lshl_add_u64 v[140:141], v[140:141], 0, v[148:149]
	global_store_dwordx4 v[140:141], v[144:147], off
